# v68 + dropped the compiler's s_waitcnt vmcnt(0) at the entry of each attention unit (only weight-copy store acknowledgements outstanding there)
# speedup vs baseline: 1.0028x; 1.0028x over previous
.LBB6_1210:
	s_cmp_ge_u32 s84, 0x200
	s_cbranch_scc1 .LBB6_1306
	s_and_b32 s0, s84, 8
	s_or_b32 s0, s0, s59
	s_sub_i32 s37, 7, s92
	s_lshr_b32 s36, s0, 2
	s_mov_b64 s[6:7], -1
	s_mov_b64 s[2:3], 0
	s_cmp_lt_i32 s93, 1
	s_mov_b64 s[4:5], 0
	s_cbranch_scc1 .LBB6_1224
	s_cmp_gt_i32 s93, 1
	s_cbranch_scc0 .LBB6_1252
	s_cmp_eq_u32 s93, 2
	s_mov_b64 s[4:5], -1
	s_cbranch_scc0 .LBB6_1251
	s_lshl_b32 s1, s37, 8
	s_lshl_b32 s6, s36, 11
	v_readlane_b32 s4, v254, 13
	s_add_i32 s0, s1, 0x100
	s_add_i32 s26, s1, s6
	v_readlane_b32 s5, v254, 14
	s_lshr_b32 s0, s0, 6
	s_mul_i32 s7, s26, 0x600
	s_mul_hi_u32 s6, s26, 0x600
	s_add_u32 s7, s4, s7
	s_addc_u32 s6, s5, s6
	s_add_u32 s7, s7, s71
	s_addc_u32 s6, s6, 0
	s_add_u32 s12, s7, 0x7200000
	s_addc_u32 s13, s6, 0
	s_mul_i32 s6, s36, 0x300000
	s_add_u32 s6, s4, s6
	s_addc_u32 s7, s5, 0
	s_add_u32 s6, s6, s71
	s_addc_u32 s7, s7, 0
	s_add_u32 s6, s6, 0x7e00000
	s_addc_u32 s7, s7, 0
	s_add_u32 s24, s4, s75
	s_addc_u32 s25, s5, 0
	s_lshl_b32 s27, s36, 12
	s_add_u32 s24, s24, s27
	v_mov_b32_e32 v183, v0
	s_addc_u32 s25, s25, 0
	v_mov_b32_e32 v34, v0
	s_add_u32 s24, s24, 0xf300000
	s_addc_u32 s25, s25, 0
	v_readfirstlane_b32 s27, v34
	s_ashr_i32 s27, s27, 1
	s_movk_i32 s28, 0xffe0
	v_mov_b32_e32 v2, s27
	v_bfi_b32 v2, s28, v2, v34
	v_mov_b64_e32 v[4:5], s[12:13]
	v_bfe_u32 v35, v34, 5, 1
	v_mad_i64_i32 v[4:5], s[12:13], v2, s70, v[4:5]
	v_lshlrev_b32_e32 v2, 4, v35
	s_mov_b32 s12, 0x2aaaaaab
	v_lshl_add_u64 v[24:25], v[4:5], 0, v[2:3]
	v_mul_hi_i32 v4, v34, s12
	v_lshrrev_b32_e32 v5, 31, v4
	v_ashrrev_i32_e32 v4, 2, v4
	v_add_u32_e32 v189, v4, v5
	v_mul_lo_u32 v4, v189, 24
	v_sub_u32_e32 v36, v34, v4
	v_add_u32_e32 v4, 0x200, v34
	v_mul_hi_i32 v5, v4, s12
	v_lshrrev_b32_e32 v6, 31, v5
	v_ashrrev_i32_e32 v5, 2, v5
	v_add_u32_e32 v190, v5, v6
	v_mul_lo_u32 v5, v190, 24
	v_sub_u32_e32 v37, v4, v5
	v_add_u32_e32 v4, 0x400, v34
	v_mul_hi_i32 v5, v4, s12
	v_lshrrev_b32_e32 v6, 31, v5
	v_ashrrev_i32_e32 v5, 2, v5
	v_add_u32_e32 v192, v5, v6
	v_mul_lo_u32 v5, v192, 24
	v_sub_u32_e32 v38, v4, v5
	v_lshlrev_b32_e32 v14, 3, v38
	v_ashrrev_i32_e32 v15, 31, v14
	v_lshlrev_b32_e32 v6, 3, v36
	v_lshlrev_b32_e32 v8, 3, v37
	v_lshlrev_b64 v[32:33], 1, v[14:15]
	v_lshlrev_b32_e32 v14, 4, v34
	v_ashrrev_i32_e32 v39, 3, v34
	v_mov_b64_e32 v[26:27], s[6:7]
	v_ashrrev_i32_e32 v7, 31, v6
	v_ashrrev_i32_e32 v9, 31, v8
	v_and_b32_e32 v168, 0x70, v14
	v_mov_b32_e32 v169, v3
	v_mad_i64_i32 v[4:5], s[12:13], v189, s70, v[26:27]
	v_lshlrev_b64 v[28:29], 1, v[6:7]
	v_mad_i64_i32 v[6:7], s[12:13], v190, s70, v[26:27]
	v_lshlrev_b64 v[30:31], 1, v[8:9]
	v_mad_i64_i32 v[12:13], s[12:13], v192, s70, v[26:27]
	v_lshl_add_u64 v[170:171], s[24:25], 0, v[168:169]
	v_add_u32_e32 v40, 64, v39
	v_lshl_add_u64 v[4:5], v[4:5], 0, v[28:29]
	v_lshl_add_u64 v[8:9], v[6:7], 0, v[30:31]
	v_lshl_add_u64 v[12:13], v[12:13], 0, v[32:33]
	v_mad_i64_i32 v[16:17], s[12:13], v39, s55, v[170:171]
	v_mad_i64_i32 v[20:21], s[12:13], v40, s55, v[170:171]
	global_load_dwordx4 v[4:7], v[4:5], off
	s_nop 0
	global_load_dwordx4 v[8:11], v[8:9], off
	s_nop 0
	global_load_dwordx4 v[12:15], v[12:13], off
	s_nop 0
	global_load_dwordx4 v[16:19], v[16:17], off
	s_nop 0
	global_load_dwordx4 v[20:23], v[20:21], off
	s_nop 0
	global_load_dwordx4 v[144:147], v[24:25], off
	global_load_dwordx4 v[140:143], v[24:25], off offset:32
	global_load_dwordx4 v[136:139], v[24:25], off offset:64
	global_load_dwordx4 v[132:135], v[24:25], off offset:96
	global_load_dwordx4 v[128:131], v[24:25], off offset:128
	global_load_dwordx4 v[124:127], v[24:25], off offset:160
	global_load_dwordx4 v[120:123], v[24:25], off offset:192
	global_load_dwordx4 v[116:119], v[24:25], off offset:224
	global_load_dwordx4 v[112:115], v[24:25], off offset:256
	global_load_dwordx4 v[108:111], v[24:25], off offset:288
	global_load_dwordx4 v[104:107], v[24:25], off offset:320
	global_load_dwordx4 v[100:103], v[24:25], off offset:352
	v_add_u32_e32 v24, 64, v189
	v_mad_i64_i32 v[24:25], s[12:13], v24, s70, v[26:27]
	v_lshl_add_u64 v[24:25], v[24:25], 0, v[28:29]
	global_load_dwordx4 v[148:151], v[24:25], off
	v_add_u32_e32 v24, 64, v190
	v_mad_i64_i32 v[24:25], s[12:13], v24, s70, v[26:27]
	v_add_u32_e32 v41, 64, v192
	v_lshl_add_u64 v[24:25], v[24:25], 0, v[30:31]
	v_mad_i64_i32 v[26:27], s[12:13], v41, s70, v[26:27]
	v_lshl_add_u64 v[26:27], v[26:27], 0, v[32:33]
	global_load_dwordx4 v[152:155], v[24:25], off
	global_load_dwordx4 v[156:159], v[26:27], off
	v_mov_b64_e32 v[24:25], s[24:25]
	v_mad_i64_i32 v[26:27], s[12:13], v39, s55, v[24:25]
	v_lshl_add_u64 v[26:27], v[26:27], 0, v[168:169]
	v_mad_i64_i32 v[24:25], s[12:13], v40, s55, v[24:25]
	v_lshl_add_u64 v[24:25], v[24:25], 0, v[168:169]
	global_load_dwordx4 v[160:163], v[26:27], off offset:128
	global_load_dwordx4 v[164:167], v[24:25], off offset:128
	s_and_b32 s25, s27, 0xffffffe0
	s_add_i32 s12, s25, s1
	v_lshlrev_b32_e32 v24, 1, v34
	v_lshrrev_b32_e32 v25, 1, v34
	s_movk_i32 s1, 0x190
	v_and_b32_e32 v24, 8, v24
	v_and_b32_e32 v25, 4, v25
	v_and_b32_e32 v26, 19, v34
	v_mul_lo_u32 v194, v189, s1
	v_lshlrev_b32_e32 v195, 4, v36
	v_or3_b32 v24, v24, v26, v25
	v_add3_u32 v25, 0, v194, v195
	v_mul_lo_u32 v196, v190, s1
	v_lshlrev_b32_e32 v197, 4, v37
	v_mul_lo_u32 v198, v192, s1
	v_lshlrev_b32_e32 v199, 4, v38
	v_mul_lo_u32 v201, v39, s41
	v_and_b32_e32 v191, 31, v34
	v_mul_i32_i24_e32 v193, -8, v35
	s_lshl_b32 s1, s92, 8
	v_mad_i64_i32 v[172:173], s[28:29], v39, s55, 0
	v_mad_i64_i32 v[174:175], s[28:29], v40, s55, 0
	v_mul_u32_u24_e32 v200, 0x190, v24
	v_lshl_add_u64 v[176:177], s[6:7], 0, v[28:29]
	v_lshl_add_u64 v[178:179], s[6:7], 0, v[30:31]
	v_lshl_add_u64 v[184:185], s[6:7], 0, v[32:33]
	s_mov_b32 s24, 1
	s_or_b32 s13, s12, 31
	v_mul_u32_u24_e32 v169, 0x90, v191
	v_mov_b32_e32 v187, 0
	v_mov_b32_e32 v188, 0xf149f2ca
	s_movk_i32 s84, 0x80
	s_waitcnt vmcnt(21)
	ds_write_b128 v25, v[4:7]
	v_add3_u32 v4, 0, v196, v197
	s_waitcnt vmcnt(20)
	ds_write_b128 v4, v[8:11]
	v_add3_u32 v4, 0, v198, v199
	s_waitcnt vmcnt(19)
	ds_write_b128 v4, v[12:15]
	v_add3_u32 v4, 0, v168, v201
	s_waitcnt vmcnt(18)
	ds_write_b128 v4, v[16:19] offset:25600
	s_waitcnt vmcnt(17)
	ds_write_b128 v4, v[20:23] offset:34816
	v_add3_u32 v4, v193, s25, v191
	v_subrev_u32_e32 v4, s1, v4
	v_mov_b32_e32 v18, v3
	v_mov_b32_e32 v19, v3
	v_add_u32_e32 v202, 0x6e9, v4
	v_mov_b32_e32 v4, v3
	v_mov_b32_e32 v5, v3
	v_mov_b32_e32 v6, v3
	v_mov_b32_e32 v7, v3
	v_mov_b32_e32 v8, v3
	v_mov_b32_e32 v9, v3
	v_mov_b32_e32 v10, v3
	v_mov_b32_e32 v11, v3
	v_mov_b32_e32 v12, v3
	v_mov_b32_e32 v13, v3
	v_mov_b32_e32 v14, v3
	v_mov_b32_e32 v15, v3
	v_mov_b32_e32 v16, v3
	v_mov_b32_e32 v17, v3
	v_mov_b64_e32 v[34:35], v[18:19]
	v_mov_b64_e32 v[50:51], v[18:19]
	v_mov_b64_e32 v[66:67], v[18:19]
	v_mov_b64_e32 v[32:33], v[16:17]
	v_mov_b64_e32 v[30:31], v[14:15]
	v_mov_b64_e32 v[28:29], v[12:13]
	v_mov_b64_e32 v[26:27], v[10:11]
	v_mov_b64_e32 v[24:25], v[8:9]
	v_mov_b64_e32 v[22:23], v[6:7]
	v_mov_b64_e32 v[20:21], v[4:5]
	v_mov_b64_e32 v[48:49], v[16:17]
	v_mov_b64_e32 v[46:47], v[14:15]
	v_mov_b64_e32 v[44:45], v[12:13]
	v_mov_b64_e32 v[42:43], v[10:11]
	v_mov_b64_e32 v[40:41], v[8:9]
	v_mov_b64_e32 v[38:39], v[6:7]
	v_mov_b64_e32 v[36:37], v[4:5]
	v_mov_b64_e32 v[64:65], v[16:17]
	v_mov_b64_e32 v[62:63], v[14:15]
	v_mov_b64_e32 v[60:61], v[12:13]
	v_mov_b64_e32 v[58:59], v[10:11]
	v_mov_b64_e32 v[56:57], v[8:9]
	v_mov_b64_e32 v[54:55], v[6:7]
	v_mov_b64_e32 v[52:53], v[4:5]
	s_waitcnt lgkmcnt(0)
	s_barrier
